# K1 scan: fully interleaved 1KiB mapping (chip sweeps one contiguous window), ring 16; hand-written agg
# baseline (speedup 1.0000x reference)
.Lk1_scan:
	s_load_dwordx2 s[4:5], s[0:1], 0x0
	s_load_dwordx4 s[8:11], s[0:1], 0x20
	s_load_dwordx2 s[12:13], s[0:1], 0x30
	v_and_b32_e32 v6, 63, v0
	v_readfirstlane_b32 s3, v0
	v_lshlrev_b32_e32 v1, 4, v6
	v_lshlrev_b32_e32 v2, 2, v6
	v_or_b32_e32 v3, 1, v2
	v_or_b32_e32 v4, 2, v2
	v_or_b32_e32 v5, 3, v2
	s_lshr_b32 s3, s3, 6
	s_sub_u32 s16, s2, 0x60
	s_lshl_b32 s16, s16, 2
	s_add_u32 s16, s16, s3
	s_mul_i32 s17, s16, 0x400
	s_lshr_b32 s18, s17, 2
	s_lshl_b32 s24, s3, 13
	s_mov_b32 s25, s24
	s_mov_b32 s28, s24
	s_mov_b32 s36, 0
	v_mov_b32_e32 v21, 1
	s_mov_b32 s27, 0
	s_mov_b32 s29, 0x55555556
	s_mov_b32 s31, 0xc0000
	s_waitcnt lgkmcnt(0)
	s_add_u32 s6, s4, s17
	s_addc_u32 s7, s5, 0
	global_load_dwordx4 v[28:31], v1, s[6:7] nt
	s_add_u32 s6, s6, 0x200000
	s_addc_u32 s7, s7, 0
	global_load_dwordx4 v[32:35], v1, s[6:7] nt
	s_add_u32 s6, s6, 0x200000
	s_addc_u32 s7, s7, 0
	global_load_dwordx4 v[36:39], v1, s[6:7] nt
	s_add_u32 s6, s6, 0x200000
	s_addc_u32 s7, s7, 0
	global_load_dwordx4 v[40:43], v1, s[6:7] nt
	s_add_u32 s6, s6, 0x200000
	s_addc_u32 s7, s7, 0
	global_load_dwordx4 v[44:47], v1, s[6:7] nt
	s_add_u32 s6, s6, 0x200000
	s_addc_u32 s7, s7, 0
	global_load_dwordx4 v[48:51], v1, s[6:7] nt
	s_add_u32 s6, s6, 0x200000
	s_addc_u32 s7, s7, 0
	global_load_dwordx4 v[52:55], v1, s[6:7] nt
	s_add_u32 s6, s6, 0x200000
	s_addc_u32 s7, s7, 0
	global_load_dwordx4 v[56:59], v1, s[6:7] nt
	s_add_u32 s6, s6, 0x200000
	s_addc_u32 s7, s7, 0
	global_load_dwordx4 v[60:63], v1, s[6:7] nt
	s_add_u32 s6, s6, 0x200000
	s_addc_u32 s7, s7, 0
	global_load_dwordx4 v[64:67], v1, s[6:7] nt
	s_add_u32 s6, s6, 0x200000
	s_addc_u32 s7, s7, 0
	global_load_dwordx4 v[68:71], v1, s[6:7] nt
	s_add_u32 s6, s6, 0x200000
	s_addc_u32 s7, s7, 0
	global_load_dwordx4 v[72:75], v1, s[6:7] nt
	s_add_u32 s6, s6, 0x200000
	s_addc_u32 s7, s7, 0
	global_load_dwordx4 v[76:79], v1, s[6:7] nt
	s_add_u32 s6, s6, 0x200000
	s_addc_u32 s7, s7, 0
	global_load_dwordx4 v[80:83], v1, s[6:7] nt
	s_add_u32 s6, s6, 0x200000
	s_addc_u32 s7, s7, 0
	global_load_dwordx4 v[84:87], v1, s[6:7] nt
	s_add_u32 s6, s6, 0x200000
	s_addc_u32 s7, s7, 0
	global_load_dwordx4 v[88:91], v1, s[6:7] nt
	s_add_u32 s6, s6, 0x200000
	s_addc_u32 s7, s7, 0
	s_mov_b32 s26, 18
.Lk1_main:
	s_waitcnt vmcnt(15)
	v_or3_b32 v12, v28, v29, v30
	v_or_b32_e32 v12, v12, v31
	v_cmp_ne_u32_e32 vcc, 0, v12
	s_cbranch_vccnz .Lk1_hitm_0
.Lk1_contm_0:
	global_load_dwordx4 v[28:31], v1, s[6:7] nt
	s_add_u32 s6, s6, 0x200000
	s_addc_u32 s7, s7, 0
	s_waitcnt vmcnt(15)
	v_or3_b32 v12, v32, v33, v34
	v_or_b32_e32 v12, v12, v35
	v_cmp_ne_u32_e32 vcc, 0, v12
	s_cbranch_vccnz .Lk1_hitm_1
.Lk1_contm_1:
	global_load_dwordx4 v[32:35], v1, s[6:7] nt
	s_add_u32 s6, s6, 0x200000
	s_addc_u32 s7, s7, 0
	s_waitcnt vmcnt(15)
	v_or3_b32 v12, v36, v37, v38
	v_or_b32_e32 v12, v12, v39
	v_cmp_ne_u32_e32 vcc, 0, v12
	s_cbranch_vccnz .Lk1_hitm_2
.Lk1_contm_2:
	global_load_dwordx4 v[36:39], v1, s[6:7] nt
	s_add_u32 s6, s6, 0x200000
	s_addc_u32 s7, s7, 0
	s_waitcnt vmcnt(15)
	v_or3_b32 v12, v40, v41, v42
	v_or_b32_e32 v12, v12, v43
	v_cmp_ne_u32_e32 vcc, 0, v12
	s_cbranch_vccnz .Lk1_hitm_3
.Lk1_contm_3:
	global_load_dwordx4 v[40:43], v1, s[6:7] nt
	s_add_u32 s6, s6, 0x200000
	s_addc_u32 s7, s7, 0
	s_waitcnt vmcnt(15)
	v_or3_b32 v12, v44, v45, v46
	v_or_b32_e32 v12, v12, v47
	v_cmp_ne_u32_e32 vcc, 0, v12
	s_cbranch_vccnz .Lk1_hitm_4
.Lk1_contm_4:
	global_load_dwordx4 v[44:47], v1, s[6:7] nt
	s_add_u32 s6, s6, 0x200000
	s_addc_u32 s7, s7, 0
	s_waitcnt vmcnt(15)
	v_or3_b32 v12, v48, v49, v50
	v_or_b32_e32 v12, v12, v51
	v_cmp_ne_u32_e32 vcc, 0, v12
	s_cbranch_vccnz .Lk1_hitm_5
.Lk1_contm_5:
	global_load_dwordx4 v[48:51], v1, s[6:7] nt
	s_add_u32 s6, s6, 0x200000
	s_addc_u32 s7, s7, 0
	s_waitcnt vmcnt(15)
	v_or3_b32 v12, v52, v53, v54
	v_or_b32_e32 v12, v12, v55
	v_cmp_ne_u32_e32 vcc, 0, v12
	s_cbranch_vccnz .Lk1_hitm_6
.Lk1_contm_6:
	global_load_dwordx4 v[52:55], v1, s[6:7] nt
	s_add_u32 s6, s6, 0x200000
	s_addc_u32 s7, s7, 0
	s_waitcnt vmcnt(15)
	v_or3_b32 v12, v56, v57, v58
	v_or_b32_e32 v12, v12, v59
	v_cmp_ne_u32_e32 vcc, 0, v12
	s_cbranch_vccnz .Lk1_hitm_7
.Lk1_contm_7:
	global_load_dwordx4 v[56:59], v1, s[6:7] nt
	s_add_u32 s6, s6, 0x200000
	s_addc_u32 s7, s7, 0
	s_waitcnt vmcnt(15)
	v_or3_b32 v12, v60, v61, v62
	v_or_b32_e32 v12, v12, v63
	v_cmp_ne_u32_e32 vcc, 0, v12
	s_cbranch_vccnz .Lk1_hitm_8
.Lk1_contm_8:
	global_load_dwordx4 v[60:63], v1, s[6:7] nt
	s_add_u32 s6, s6, 0x200000
	s_addc_u32 s7, s7, 0
	s_waitcnt vmcnt(15)
	v_or3_b32 v12, v64, v65, v66
	v_or_b32_e32 v12, v12, v67
	v_cmp_ne_u32_e32 vcc, 0, v12
	s_cbranch_vccnz .Lk1_hitm_9
.Lk1_contm_9:
	global_load_dwordx4 v[64:67], v1, s[6:7] nt
	s_add_u32 s6, s6, 0x200000
	s_addc_u32 s7, s7, 0
	s_waitcnt vmcnt(15)
	v_or3_b32 v12, v68, v69, v70
	v_or_b32_e32 v12, v12, v71
	v_cmp_ne_u32_e32 vcc, 0, v12
	s_cbranch_vccnz .Lk1_hitm_10
.Lk1_contm_10:
	global_load_dwordx4 v[68:71], v1, s[6:7] nt
	s_add_u32 s6, s6, 0x200000
	s_addc_u32 s7, s7, 0
	s_waitcnt vmcnt(15)
	v_or3_b32 v12, v72, v73, v74
	v_or_b32_e32 v12, v12, v75
	v_cmp_ne_u32_e32 vcc, 0, v12
	s_cbranch_vccnz .Lk1_hitm_11
.Lk1_contm_11:
	global_load_dwordx4 v[72:75], v1, s[6:7] nt
	s_add_u32 s6, s6, 0x200000
	s_addc_u32 s7, s7, 0
	s_waitcnt vmcnt(15)
	v_or3_b32 v12, v76, v77, v78
	v_or_b32_e32 v12, v12, v79
	v_cmp_ne_u32_e32 vcc, 0, v12
	s_cbranch_vccnz .Lk1_hitm_12
.Lk1_contm_12:
	global_load_dwordx4 v[76:79], v1, s[6:7] nt
	s_add_u32 s6, s6, 0x200000
	s_addc_u32 s7, s7, 0
	s_waitcnt vmcnt(15)
	v_or3_b32 v12, v80, v81, v82
	v_or_b32_e32 v12, v12, v83
	v_cmp_ne_u32_e32 vcc, 0, v12
	s_cbranch_vccnz .Lk1_hitm_13
.Lk1_contm_13:
	global_load_dwordx4 v[80:83], v1, s[6:7] nt
	s_add_u32 s6, s6, 0x200000
	s_addc_u32 s7, s7, 0
	s_waitcnt vmcnt(15)
	v_or3_b32 v12, v84, v85, v86
	v_or_b32_e32 v12, v12, v87
	v_cmp_ne_u32_e32 vcc, 0, v12
	s_cbranch_vccnz .Lk1_hitm_14
.Lk1_contm_14:
	global_load_dwordx4 v[84:87], v1, s[6:7] nt
	s_add_u32 s6, s6, 0x200000
	s_addc_u32 s7, s7, 0
	s_waitcnt vmcnt(15)
	v_or3_b32 v12, v88, v89, v90
	v_or_b32_e32 v12, v12, v91
	v_cmp_ne_u32_e32 vcc, 0, v12
	s_cbranch_vccnz .Lk1_hitm_15
.Lk1_contm_15:
	global_load_dwordx4 v[88:91], v1, s[6:7] nt
	s_add_u32 s6, s6, 0x200000
	s_addc_u32 s7, s7, 0
	s_add_u32 s18, s18, 0x800000
	s_sub_u32 s26, s26, 1
	s_cmp_lg_u32 s26, 1
	s_cbranch_scc1 .Lk1_main
	s_waitcnt vmcnt(15)
	v_or3_b32 v12, v28, v29, v30
	v_or_b32_e32 v12, v12, v31
	v_cmp_ne_u32_e32 vcc, 0, v12
	s_cbranch_vccnz .Lk1_hitl_0
.Lk1_contl_0:
	s_waitcnt vmcnt(14)
	v_or3_b32 v12, v32, v33, v34
	v_or_b32_e32 v12, v12, v35
	v_cmp_ne_u32_e32 vcc, 0, v12
	s_cbranch_vccnz .Lk1_hitl_1
.Lk1_contl_1:
	s_waitcnt vmcnt(13)
	v_or3_b32 v12, v36, v37, v38
	v_or_b32_e32 v12, v12, v39
	v_cmp_ne_u32_e32 vcc, 0, v12
	s_cbranch_vccnz .Lk1_hitl_2
.Lk1_contl_2:
	s_waitcnt vmcnt(12)
	v_or3_b32 v12, v40, v41, v42
	v_or_b32_e32 v12, v12, v43
	v_cmp_ne_u32_e32 vcc, 0, v12
	s_cbranch_vccnz .Lk1_hitl_3
.Lk1_contl_3:
	s_waitcnt vmcnt(11)
	v_or3_b32 v12, v44, v45, v46
	v_or_b32_e32 v12, v12, v47
	v_cmp_ne_u32_e32 vcc, 0, v12
	s_cbranch_vccnz .Lk1_hitl_4
.Lk1_contl_4:
	s_waitcnt vmcnt(10)
	v_or3_b32 v12, v48, v49, v50
	v_or_b32_e32 v12, v12, v51
	v_cmp_ne_u32_e32 vcc, 0, v12
	s_cbranch_vccnz .Lk1_hitl_5
.Lk1_contl_5:
	s_waitcnt vmcnt(9)
	v_or3_b32 v12, v52, v53, v54
	v_or_b32_e32 v12, v12, v55
	v_cmp_ne_u32_e32 vcc, 0, v12
	s_cbranch_vccnz .Lk1_hitl_6
.Lk1_contl_6:
	s_waitcnt vmcnt(8)
	v_or3_b32 v12, v56, v57, v58
	v_or_b32_e32 v12, v12, v59
	v_cmp_ne_u32_e32 vcc, 0, v12
	s_cbranch_vccnz .Lk1_hitl_7
.Lk1_contl_7:
	s_waitcnt vmcnt(7)
	v_or3_b32 v12, v60, v61, v62
	v_or_b32_e32 v12, v12, v63
	v_cmp_ne_u32_e32 vcc, 0, v12
	s_cbranch_vccnz .Lk1_hitl_8
.Lk1_contl_8:
	s_waitcnt vmcnt(6)
	v_or3_b32 v12, v64, v65, v66
	v_or_b32_e32 v12, v12, v67
	v_cmp_ne_u32_e32 vcc, 0, v12
	s_cbranch_vccnz .Lk1_hitl_9
.Lk1_contl_9:
	s_waitcnt vmcnt(5)
	v_or3_b32 v12, v68, v69, v70
	v_or_b32_e32 v12, v12, v71
	v_cmp_ne_u32_e32 vcc, 0, v12
	s_cbranch_vccnz .Lk1_hitl_10
.Lk1_contl_10:
	s_waitcnt vmcnt(4)
	v_or3_b32 v12, v72, v73, v74
	v_or_b32_e32 v12, v12, v75
	v_cmp_ne_u32_e32 vcc, 0, v12
	s_cbranch_vccnz .Lk1_hitl_11
.Lk1_contl_11:
	s_waitcnt vmcnt(3)
	v_or3_b32 v12, v76, v77, v78
	v_or_b32_e32 v12, v12, v79
	v_cmp_ne_u32_e32 vcc, 0, v12
	s_cbranch_vccnz .Lk1_hitl_12
.Lk1_contl_12:
	s_waitcnt vmcnt(2)
	v_or3_b32 v12, v80, v81, v82
	v_or_b32_e32 v12, v12, v83
	v_cmp_ne_u32_e32 vcc, 0, v12
	s_cbranch_vccnz .Lk1_hitl_13
.Lk1_contl_13:
	s_waitcnt vmcnt(1)
	v_or3_b32 v12, v84, v85, v86
	v_or_b32_e32 v12, v12, v87
	v_cmp_ne_u32_e32 vcc, 0, v12
	s_cbranch_vccnz .Lk1_hitl_14
.Lk1_contl_14:
	s_waitcnt vmcnt(0)
	v_or3_b32 v12, v88, v89, v90
	v_or_b32_e32 v12, v12, v91
	v_cmp_ne_u32_e32 vcc, 0, v12
	s_cbranch_vccnz .Lk1_hitl_15

.Lk1_hitm_1:
	v_mov_b32_e32 v8, v32
	v_mov_b32_e32 v9, v33
	v_mov_b32_e32 v10, v34
	v_mov_b32_e32 v11, v35
	s_add_u32 s19, s18, 0x80000
	s_movk_i32 s23, 1
	s_branch .Lk1_slow
.Lk1_hitm_2:
	v_mov_b32_e32 v8, v36
	v_mov_b32_e32 v9, v37
	v_mov_b32_e32 v10, v38
	v_mov_b32_e32 v11, v39
	s_add_u32 s19, s18, 0x100000
	s_movk_i32 s23, 2
	s_branch .Lk1_slow
.Lk1_hitm_3:
	v_mov_b32_e32 v8, v40
	v_mov_b32_e32 v9, v41
	v_mov_b32_e32 v10, v42
	v_mov_b32_e32 v11, v43
	s_add_u32 s19, s18, 0x180000
	s_movk_i32 s23, 3
	s_branch .Lk1_slow
.Lk1_hitm_4:
	v_mov_b32_e32 v8, v44
	v_mov_b32_e32 v9, v45
	v_mov_b32_e32 v10, v46
	v_mov_b32_e32 v11, v47
	s_add_u32 s19, s18, 0x200000
	s_movk_i32 s23, 4
	s_branch .Lk1_slow
.Lk1_hitm_5:
	v_mov_b32_e32 v8, v48
	v_mov_b32_e32 v9, v49
	v_mov_b32_e32 v10, v50
	v_mov_b32_e32 v11, v51
	s_add_u32 s19, s18, 0x280000
	s_movk_i32 s23, 5
	s_branch .Lk1_slow
.Lk1_hitm_6:
	v_mov_b32_e32 v8, v52
	v_mov_b32_e32 v9, v53
	v_mov_b32_e32 v10, v54
	v_mov_b32_e32 v11, v55
	s_add_u32 s19, s18, 0x300000
	s_movk_i32 s23, 6
	s_branch .Lk1_slow
.Lk1_hitm_7:
	v_mov_b32_e32 v8, v56
	v_mov_b32_e32 v9, v57
	v_mov_b32_e32 v10, v58
	v_mov_b32_e32 v11, v59
	s_add_u32 s19, s18, 0x380000
	s_movk_i32 s23, 7
	s_branch .Lk1_slow
.Lk1_hitm_8:
	v_mov_b32_e32 v8, v60
	v_mov_b32_e32 v9, v61
	v_mov_b32_e32 v10, v62
	v_mov_b32_e32 v11, v63
	s_add_u32 s19, s18, 0x400000
	s_movk_i32 s23, 8
	s_branch .Lk1_slow
.Lk1_hitm_9:
	v_mov_b32_e32 v8, v64
	v_mov_b32_e32 v9, v65
	v_mov_b32_e32 v10, v66
	v_mov_b32_e32 v11, v67
	s_add_u32 s19, s18, 0x480000
	s_movk_i32 s23, 9
	s_branch .Lk1_slow
.Lk1_hitm_10:
	v_mov_b32_e32 v8, v68
	v_mov_b32_e32 v9, v69
	v_mov_b32_e32 v10, v70
	v_mov_b32_e32 v11, v71
	s_add_u32 s19, s18, 0x500000
	s_movk_i32 s23, 10
	s_branch .Lk1_slow
.Lk1_hitm_11:
	v_mov_b32_e32 v8, v72
	v_mov_b32_e32 v9, v73
	v_mov_b32_e32 v10, v74
	v_mov_b32_e32 v11, v75
	s_add_u32 s19, s18, 0x580000
	s_movk_i32 s23, 11
	s_branch .Lk1_slow
.Lk1_hitm_12:
	v_mov_b32_e32 v8, v76
	v_mov_b32_e32 v9, v77
	v_mov_b32_e32 v10, v78
	v_mov_b32_e32 v11, v79
	s_add_u32 s19, s18, 0x600000
	s_movk_i32 s23, 12
	s_branch .Lk1_slow
.Lk1_hitm_13:
	v_mov_b32_e32 v8, v80
	v_mov_b32_e32 v9, v81
	v_mov_b32_e32 v10, v82
	v_mov_b32_e32 v11, v83
	s_add_u32 s19, s18, 0x680000
	s_movk_i32 s23, 13
	s_branch .Lk1_slow
.Lk1_hitm_14:
	v_mov_b32_e32 v8, v84
	v_mov_b32_e32 v9, v85
	v_mov_b32_e32 v10, v86
	v_mov_b32_e32 v11, v87
	s_add_u32 s19, s18, 0x700000
	s_movk_i32 s23, 14
	s_branch .Lk1_slow
.Lk1_hitm_15:
	v_mov_b32_e32 v8, v88
	v_mov_b32_e32 v9, v89
	v_mov_b32_e32 v10, v90
	v_mov_b32_e32 v11, v91
	s_add_u32 s19, s18, 0x780000
	s_movk_i32 s23, 15
	s_branch .Lk1_slow
.Lk1_hitl_0:
	v_mov_b32_e32 v8, v28
	v_mov_b32_e32 v9, v29
	v_mov_b32_e32 v10, v30
	v_mov_b32_e32 v11, v31
	s_mov_b32 s19, s18
	s_movk_i32 s23, 16
	s_branch .Lk1_slow
.Lk1_hitl_1:
	v_mov_b32_e32 v8, v32
	v_mov_b32_e32 v9, v33
	v_mov_b32_e32 v10, v34
	v_mov_b32_e32 v11, v35
	s_add_u32 s19, s18, 0x80000
	s_movk_i32 s23, 17
	s_branch .Lk1_slow
.Lk1_hitl_2:
	v_mov_b32_e32 v8, v36
	v_mov_b32_e32 v9, v37
	v_mov_b32_e32 v10, v38
	v_mov_b32_e32 v11, v39
	s_add_u32 s19, s18, 0x100000
	s_movk_i32 s23, 18
	s_branch .Lk1_slow
.Lk1_hitl_3:
	v_mov_b32_e32 v8, v40
	v_mov_b32_e32 v9, v41
	v_mov_b32_e32 v10, v42
	v_mov_b32_e32 v11, v43
	s_add_u32 s19, s18, 0x180000
	s_movk_i32 s23, 19
	s_branch .Lk1_slow
.Lk1_hitl_4:
	v_mov_b32_e32 v8, v44
	v_mov_b32_e32 v9, v45
	v_mov_b32_e32 v10, v46
	v_mov_b32_e32 v11, v47
	s_add_u32 s19, s18, 0x200000
	s_movk_i32 s23, 20
	s_branch .Lk1_slow
.Lk1_hitl_5:
	v_mov_b32_e32 v8, v48
	v_mov_b32_e32 v9, v49
	v_mov_b32_e32 v10, v50
	v_mov_b32_e32 v11, v51
	s_add_u32 s19, s18, 0x280000
	s_movk_i32 s23, 21
	s_branch .Lk1_slow
.Lk1_hitl_6:
	v_mov_b32_e32 v8, v52
	v_mov_b32_e32 v9, v53
	v_mov_b32_e32 v10, v54
	v_mov_b32_e32 v11, v55
	s_add_u32 s19, s18, 0x300000
	s_movk_i32 s23, 22
	s_branch .Lk1_slow
.Lk1_hitl_7:
	v_mov_b32_e32 v8, v56
	v_mov_b32_e32 v9, v57
	v_mov_b32_e32 v10, v58
	v_mov_b32_e32 v11, v59
	s_add_u32 s19, s18, 0x380000
	s_movk_i32 s23, 23
	s_branch .Lk1_slow
.Lk1_hitl_8:
	v_mov_b32_e32 v8, v60
	v_mov_b32_e32 v9, v61
	v_mov_b32_e32 v10, v62
	v_mov_b32_e32 v11, v63
	s_add_u32 s19, s18, 0x400000
	s_movk_i32 s23, 24
	s_branch .Lk1_slow
.Lk1_hitl_9:
	v_mov_b32_e32 v8, v64
	v_mov_b32_e32 v9, v65
	v_mov_b32_e32 v10, v66
	v_mov_b32_e32 v11, v67
	s_add_u32 s19, s18, 0x480000
	s_movk_i32 s23, 25
	s_branch .Lk1_slow
.Lk1_hitl_10:
	v_mov_b32_e32 v8, v68
	v_mov_b32_e32 v9, v69
	v_mov_b32_e32 v10, v70
	v_mov_b32_e32 v11, v71
	s_add_u32 s19, s18, 0x500000
	s_movk_i32 s23, 26
	s_branch .Lk1_slow
.Lk1_hitl_11:
	v_mov_b32_e32 v8, v72
	v_mov_b32_e32 v9, v73
	v_mov_b32_e32 v10, v74
	v_mov_b32_e32 v11, v75
	s_add_u32 s19, s18, 0x580000
	s_movk_i32 s23, 27
	s_branch .Lk1_slow
.Lk1_hitl_12:
	v_mov_b32_e32 v8, v76
	v_mov_b32_e32 v9, v77
	v_mov_b32_e32 v10, v78
	v_mov_b32_e32 v11, v79
	s_add_u32 s19, s18, 0x600000
	s_movk_i32 s23, 28
	s_branch .Lk1_slow
.Lk1_hitl_13:
	v_mov_b32_e32 v8, v80
	v_mov_b32_e32 v9, v81
	v_mov_b32_e32 v10, v82
	v_mov_b32_e32 v11, v83
	s_add_u32 s19, s18, 0x680000
	s_movk_i32 s23, 29
	s_branch .Lk1_slow
.Lk1_hitl_14:
	v_mov_b32_e32 v8, v84
	v_mov_b32_e32 v9, v85
	v_mov_b32_e32 v10, v86
	v_mov_b32_e32 v11, v87
	s_add_u32 s19, s18, 0x700000
	s_movk_i32 s23, 30
	s_branch .Lk1_slow
.Lk1_hitl_15:
	v_mov_b32_e32 v8, v88
	v_mov_b32_e32 v9, v89
	v_mov_b32_e32 v10, v90
	v_mov_b32_e32 v11, v91
	s_add_u32 s19, s18, 0x780000
	s_movk_i32 s23, 31
	s_branch .Lk1_slow

amdhsa.kernels:
  - .agpr_count:     0
    .args:
      - .actual_access:  read_only
        .address_space:  global
        .offset:         0
        .size:           8
        .value_kind:     global_buffer
      - .actual_access:  read_only
        .address_space:  global
        .offset:         8
        .size:           8
        .value_kind:     global_buffer
      - .actual_access:  read_only
        .address_space:  global
        .offset:         16
        .size:           8
        .value_kind:     global_buffer
      - .actual_access:  write_only
        .address_space:  global
        .offset:         24
        .size:           8
        .value_kind:     global_buffer
      - .address_space:  global
        .offset:         32
        .size:           8
        .value_kind:     global_buffer
      - .address_space:  global
        .offset:         40
        .size:           8
        .value_kind:     global_buffer
      - .actual_access:  write_only
        .address_space:  global
        .offset:         48
        .size:           8
        .value_kind:     global_buffer
      - .actual_access:  write_only
        .address_space:  global
        .offset:         56
        .size:           8
        .value_kind:     global_buffer
    .group_segment_fixed_size: 37392
    .kernarg_segment_align: 8
    .kernarg_segment_size: 64
    .language:       OpenCL C
    .language_version:
      - 2
      - 0
    .max_flat_workgroup_size: 256
    .name:           _Z9k1_kernelPKfS0_S0_PDF16_PiPfP15HIP_vector_typeIiLj2EES6_
    .private_segment_fixed_size: 0
    .sgpr_count:     32
    .sgpr_spill_count: 0
    .symbol:         _Z9k1_kernelPKfS0_S0_PDF16_PiPfP15HIP_vector_typeIiLj2EES6_.kd
    .uniform_work_group_size: 1
    .uses_dynamic_stack: false
    .vgpr_count:     140
    .vgpr_spill_count: 0
    .wavefront_size: 64
  - .agpr_count:     0
    .args:
      - .actual_access:  read_only
        .address_space:  global
        .offset:         0
        .size:           8
        .value_kind:     global_buffer
      - .actual_access:  read_only
        .address_space:  global
        .offset:         8
        .size:           8
        .value_kind:     global_buffer
      - .actual_access:  read_only
        .address_space:  global
        .offset:         16
        .size:           8
        .value_kind:     global_buffer
      - .actual_access:  read_only
        .address_space:  global
        .offset:         24
        .size:           8
        .value_kind:     global_buffer
      - .actual_access:  read_only
        .address_space:  global
        .offset:         32
        .size:           8
        .value_kind:     global_buffer
      - .actual_access:  read_only
        .address_space:  global
        .offset:         40
        .size:           8
        .value_kind:     global_buffer
      - .actual_access:  read_only
        .address_space:  global
        .offset:         48
        .size:           8
        .value_kind:     global_buffer
      - .actual_access:  read_only
        .address_space:  global
        .offset:         56
        .size:           8
        .value_kind:     global_buffer
      - .actual_access:  read_only
        .address_space:  global
        .offset:         64
        .size:           8
        .value_kind:     global_buffer
      - .actual_access:  write_only
        .address_space:  global
        .offset:         72
        .size:           8
        .value_kind:     global_buffer
      - .address_space:  global
        .offset:         80
        .size:           8
        .value_kind:     global_buffer
    .group_segment_fixed_size: 44224
    .kernarg_segment_align: 8
    .kernarg_segment_size: 88
    .language:       OpenCL C
    .language_version:
      - 2
      - 0
    .max_flat_workgroup_size: 512
    .name:           _Z11agg2_kernelPKiPKfPK15HIP_vector_typeIiLj2EEPKDF16_S2_S2_S2_S2_S2_PfS9_
    .private_segment_fixed_size: 0
    .sgpr_count:     41
    .sgpr_spill_count: 0
    .symbol:         _Z11agg2_kernelPKiPKfPK15HIP_vector_typeIiLj2EEPKDF16_S2_S2_S2_S2_S2_PfS9_.kd
    .uniform_work_group_size: 1
    .uses_dynamic_stack: false
    .vgpr_count:     80
    .vgpr_spill_count: 0
    .wavefront_size: 64
  - .agpr_count:     0
    .args:
      - .actual_access:  read_only
        .address_space:  global
        .offset:         0
        .size:           8
        .value_kind:     global_buffer
      - .actual_access:  read_only
        .address_space:  global
        .offset:         8
        .size:           8
        .value_kind:     global_buffer
      - .actual_access:  read_only
        .address_space:  global
        .offset:         16
        .size:           8
        .value_kind:     global_buffer
      - .actual_access:  read_only
        .address_space:  global
        .offset:         24
        .size:           8
        .value_kind:     global_buffer
      - .actual_access:  write_only
        .address_space:  global
        .offset:         32
        .size:           8
        .value_kind:     global_buffer
      - .offset:         40
        .size:           4
        .value_kind:     hidden_block_count_x
      - .offset:         44
        .size:           4
        .value_kind:     hidden_block_count_y
      - .offset:         48
        .size:           4
        .value_kind:     hidden_block_count_z
      - .offset:         52
        .size:           2
        .value_kind:     hidden_group_size_x
      - .offset:         54
        .size:           2
        .value_kind:     hidden_group_size_y
      - .offset:         56
        .size:           2
        .value_kind:     hidden_group_size_z
      - .offset:         58
        .size:           2
        .value_kind:     hidden_remainder_x
      - .offset:         60
        .size:           2
        .value_kind:     hidden_remainder_y
      - .offset:         62
        .size:           2
        .value_kind:     hidden_remainder_z
      - .offset:         80
        .size:           8
        .value_kind:     hidden_global_offset_x
      - .offset:         88
        .size:           8
        .value_kind:     hidden_global_offset_y
      - .offset:         96
        .size:           8
        .value_kind:     hidden_global_offset_z
      - .offset:         104
        .size:           2
        .value_kind:     hidden_grid_dims
    .group_segment_fixed_size: 512
    .kernarg_segment_align: 8
    .kernarg_segment_size: 296
    .language:       OpenCL C
    .language_version:
      - 2
      - 0
    .max_flat_workgroup_size: 256
    .name:           _Z12final_kernelPKfS0_S0_S0_Pf
    .private_segment_fixed_size: 0
    .sgpr_count:     18
    .sgpr_spill_count: 0
    .symbol:         _Z12final_kernelPKfS0_S0_S0_Pf.kd
    .uniform_work_group_size: 1
    .uses_dynamic_stack: false
    .vgpr_count:     36
    .vgpr_spill_count: 0
    .wavefront_size: 64
  - .agpr_count:     0
    .args:
      - .actual_access:  read_only
        .address_space:  global
        .offset:         0
        .size:           8
        .value_kind:     global_buffer
      - .actual_access:  read_only
        .address_space:  global
        .offset:         8
        .size:           8
        .value_kind:     global_buffer
      - .address_space:  global
        .offset:         16
        .size:           8
        .value_kind:     global_buffer
      - .address_space:  global
        .offset:         24
        .size:           8
        .value_kind:     global_buffer
      - .actual_access:  read_only
        .address_space:  global
        .offset:         32
        .size:           8
        .value_kind:     global_buffer
      - .actual_access:  read_only
        .address_space:  global
        .offset:         40
        .size:           8
        .value_kind:     global_buffer
      - .actual_access:  write_only
        .address_space:  global
        .offset:         48
        .size:           8
        .value_kind:     global_buffer
      - .address_space:  global
        .offset:         56
        .size:           8
        .value_kind:     global_buffer
    .group_segment_fixed_size: 8192
    .kernarg_segment_align: 8
    .kernarg_segment_size: 64
    .language:       OpenCL C
    .language_version:
      - 2
      - 0
    .max_flat_workgroup_size: 512
    .name:           _Z10agg_kernelILi128ELb1EEvPKiPKfP15HIP_vector_typeIiLj2EES6_PKDF16_S3_PDF16_Pf
    .private_segment_fixed_size: 0
    .sgpr_count:     66
    .sgpr_spill_count: 0
    .symbol:         _Z10agg_kernelILi128ELb1EEvPKiPKfP15HIP_vector_typeIiLj2EES6_PKDF16_S3_PDF16_Pf.kd
    .uniform_work_group_size: 1
    .uses_dynamic_stack: false
    .vgpr_count:     80
    .vgpr_spill_count: 0
    .wavefront_size: 64
